# prologue adaLN partial item: k loop hand-written with 32 row loads in flight (register FIFO, counted waits) instead of one load per wait; same FMAs and k order
# speedup vs baseline: 1.0142x; 1.0037x over previous
.LBB0_57:
	s_and_b32 s22, s39, 15
	s_lshl_b32 s23, s22, 9
	s_mul_i32 s48, s22, 0x600000
	s_ashr_i32 s22, s26, 4
	s_add_i32 s25, s23, 0
	s_mul_hi_i32 s23, s22, 0x2aaaaaab
	s_lshr_b32 s24, s23, 31
	s_lshr_b32 s23, s23, 3
	s_add_i32 s23, s23, s24
	s_mul_i32 s23, s23, 48
	s_sub_i32 s22, s22, s23
	s_mul_hi_i32 s23, s26, 0x2aaaaaab
	s_lshr_b32 s24, s23, 31
	s_ashr_i32 s23, s23, 7
	s_add_i32 s24, s23, s24
	s_lshl_b32 s22, s22, 8
	s_ashr_i32 s23, s22, 31
	s_mul_i32 s50, s24, 0x6000000
	s_mul_hi_i32 s49, s24, 0x6000000
	s_add_u32 s48, s50, s48
	s_addc_u32 s49, s49, 0
	s_lshl_b64 s[22:23], s[22:23], 2
	s_add_u32 s48, s48, s22
	s_addc_u32 s49, s49, s23
	v_mov_b32_e32 v2, 0
	v_lshl_add_u64 v[28:29], v[46:47], 0, s[48:49]
	s_mov_b32 s48, 0
	v_mov_b32_e32 v3, v2
	v_mov_b32_e32 v4, v2
	v_mov_b32_e32 v5, v2
	v_mov_b32_e32 v18, v2
	v_mov_b32_e32 v19, v2
	v_mov_b32_e32 v20, v2
	v_mov_b32_e32 v21, v2
	v_mov_b32_e32 v14, v2
	v_mov_b32_e32 v15, v2
	v_mov_b32_e32 v16, v2
	v_mov_b32_e32 v17, v2
	v_mov_b32_e32 v10, v2
	v_mov_b32_e32 v11, v2
	v_mov_b32_e32 v12, v2
	v_mov_b32_e32 v13, v2
	v_mov_b32_e32 v6, v2
	v_mov_b32_e32 v7, v2
	v_mov_b32_e32 v8, v2
	v_mov_b32_e32 v9, v2
	v_readfirstlane_b32 s48, v28
	v_readfirstlane_b32 s49, v29
	v_mov_b32_e32 v107, s25
	v_add_u32_e32 v107, 0x12000, v107
	s_nop 1
	v_subrev_u32_e32 v106, s48, v28
	s_sub_u32 s48, s48, 0x60000
	s_subb_u32 s49, s49, 0
	s_nop 3
	global_load_dwordx4 v[108:111], v106, s[48:49] nt
	s_add_u32 s48, s48, 0xc000
	s_addc_u32 s49, s49, 0
	global_load_dwordx4 v[112:115], v106, s[48:49] nt
	s_add_u32 s48, s48, 0xc000
	s_addc_u32 s49, s49, 0
	global_load_dwordx4 v[116:119], v106, s[48:49] nt
	s_add_u32 s48, s48, 0xc000
	s_addc_u32 s49, s49, 0
	global_load_dwordx4 v[120:123], v106, s[48:49] nt
	s_add_u32 s48, s48, 0xc000
	s_addc_u32 s49, s49, 0
	global_load_dwordx4 v[124:127], v106, s[48:49] nt
	s_add_u32 s48, s48, 0xc000
	s_addc_u32 s49, s49, 0
	global_load_dwordx4 v[128:131], v106, s[48:49] nt
	s_add_u32 s48, s48, 0xc000
	s_addc_u32 s49, s49, 0
	global_load_dwordx4 v[132:135], v106, s[48:49] nt
	s_add_u32 s48, s48, 0xc000
	s_addc_u32 s49, s49, 0
	global_load_dwordx4 v[136:139], v106, s[48:49] nt
	s_add_u32 s48, s48, 0xc000
	s_addc_u32 s49, s49, 0
	global_load_dwordx4 v[140:143], v106, s[48:49] nt
	s_add_u32 s48, s48, 0xc000
	s_addc_u32 s49, s49, 0
	global_load_dwordx4 v[144:147], v106, s[48:49] nt
	s_add_u32 s48, s48, 0xc000
	s_addc_u32 s49, s49, 0
	global_load_dwordx4 v[148:151], v106, s[48:49] nt
	s_add_u32 s48, s48, 0xc000
	s_addc_u32 s49, s49, 0
	global_load_dwordx4 v[152:155], v106, s[48:49] nt
	s_add_u32 s48, s48, 0xc000
	s_addc_u32 s49, s49, 0
	global_load_dwordx4 v[156:159], v106, s[48:49] nt
	s_add_u32 s48, s48, 0xc000
	s_addc_u32 s49, s49, 0
	global_load_dwordx4 v[160:163], v106, s[48:49] nt
	s_add_u32 s48, s48, 0xc000
	s_addc_u32 s49, s49, 0
	global_load_dwordx4 v[164:167], v106, s[48:49] nt
	s_add_u32 s48, s48, 0xc000
	s_addc_u32 s49, s49, 0
	global_load_dwordx4 v[168:171], v106, s[48:49] nt
	s_add_u32 s48, s48, 0xc000
	s_addc_u32 s49, s49, 0
	global_load_dwordx4 v[172:175], v106, s[48:49] nt
	s_add_u32 s48, s48, 0xc000
	s_addc_u32 s49, s49, 0
	global_load_dwordx4 v[176:179], v106, s[48:49] nt
	s_add_u32 s48, s48, 0xc000
	s_addc_u32 s49, s49, 0
	global_load_dwordx4 v[180:183], v106, s[48:49] nt
	s_add_u32 s48, s48, 0xc000
	s_addc_u32 s49, s49, 0
	global_load_dwordx4 v[184:187], v106, s[48:49] nt
	s_add_u32 s48, s48, 0xc000
	s_addc_u32 s49, s49, 0
	global_load_dwordx4 v[188:191], v106, s[48:49] nt
	s_add_u32 s48, s48, 0xc000
	s_addc_u32 s49, s49, 0
	global_load_dwordx4 v[192:195], v106, s[48:49] nt
	s_add_u32 s48, s48, 0xc000
	s_addc_u32 s49, s49, 0
	global_load_dwordx4 v[196:199], v106, s[48:49] nt
	s_add_u32 s48, s48, 0xc000
	s_addc_u32 s49, s49, 0
	global_load_dwordx4 v[200:203], v106, s[48:49] nt
	s_add_u32 s48, s48, 0xc000
	s_addc_u32 s49, s49, 0
	global_load_dwordx4 v[204:207], v106, s[48:49] nt
	s_add_u32 s48, s48, 0xc000
	s_addc_u32 s49, s49, 0
	global_load_dwordx4 v[208:211], v106, s[48:49] nt
	s_add_u32 s48, s48, 0xc000
	s_addc_u32 s49, s49, 0
	global_load_dwordx4 v[212:215], v106, s[48:49] nt
	s_add_u32 s48, s48, 0xc000
	s_addc_u32 s49, s49, 0
	global_load_dwordx4 v[216:219], v106, s[48:49] nt
	s_add_u32 s48, s48, 0xc000
	s_addc_u32 s49, s49, 0
	global_load_dwordx4 v[220:223], v106, s[48:49] nt
	s_add_u32 s48, s48, 0xc000
	s_addc_u32 s49, s49, 0
	global_load_dwordx4 v[224:227], v106, s[48:49] nt
	s_add_u32 s48, s48, 0xc000
	s_addc_u32 s49, s49, 0
	global_load_dwordx4 v[228:231], v106, s[48:49] nt
	s_add_u32 s48, s48, 0xc000
	s_addc_u32 s49, s49, 0
	global_load_dwordx4 v[232:235], v106, s[48:49] nt
	s_add_u32 s48, s48, 0xc000
	s_addc_u32 s49, s49, 0
	ds_read_b128 v[22:25], v107 offset:0
	ds_read_b128 v[26:29], v107 offset:8192
	ds_read_b128 v[30:33], v107 offset:16384
	ds_read_b128 v[92:95], v107 offset:24576
	ds_read_b128 v[96:99], v107 offset:32768
	s_mov_b32 s50, 3
.Lada_loop:
	ds_read_b128 v[236:239], v107 offset:16
	ds_read_b128 v[240:243], v107 offset:8208
	ds_read_b128 v[244:247], v107 offset:16400
	ds_read_b128 v[248:251], v107 offset:24592
	ds_read_b128 v[100:103], v107 offset:32784
	s_waitcnt lgkmcnt(5)
	s_waitcnt vmcnt(31)
	v_pk_fma_f32 v[18:19], v[108:109], v[22:23], v[18:19] op_sel_hi:[1,0,1]
	v_pk_fma_f32 v[20:21], v[110:111], v[22:23], v[20:21] op_sel_hi:[1,0,1]
	v_pk_fma_f32 v[14:15], v[108:109], v[26:27], v[14:15] op_sel_hi:[1,0,1]
	v_pk_fma_f32 v[16:17], v[110:111], v[26:27], v[16:17] op_sel_hi:[1,0,1]
	v_pk_fma_f32 v[10:11], v[108:109], v[30:31], v[10:11] op_sel_hi:[1,0,1]
	v_pk_fma_f32 v[12:13], v[110:111], v[30:31], v[12:13] op_sel_hi:[1,0,1]
	v_pk_fma_f32 v[6:7], v[108:109], v[92:93], v[6:7] op_sel_hi:[1,0,1]
	v_pk_fma_f32 v[8:9], v[110:111], v[92:93], v[8:9] op_sel_hi:[1,0,1]
	v_pk_fma_f32 v[2:3], v[108:109], v[96:97], v[2:3] op_sel_hi:[1,0,1]
	v_pk_fma_f32 v[4:5], v[110:111], v[96:97], v[4:5] op_sel_hi:[1,0,1]
	global_load_dwordx4 v[108:111], v106, s[48:49] nt
	s_add_u32 s48, s48, 0xc000
	s_addc_u32 s49, s49, 0
	s_waitcnt vmcnt(31)
	v_pk_fma_f32 v[18:19], v[112:113], v[22:23], v[18:19] op_sel:[0,1,0]
	v_pk_fma_f32 v[20:21], v[114:115], v[22:23], v[20:21] op_sel:[0,1,0]
	v_pk_fma_f32 v[14:15], v[112:113], v[26:27], v[14:15] op_sel:[0,1,0]
	v_pk_fma_f32 v[16:17], v[114:115], v[26:27], v[16:17] op_sel:[0,1,0]
	v_pk_fma_f32 v[10:11], v[112:113], v[30:31], v[10:11] op_sel:[0,1,0]
	v_pk_fma_f32 v[12:13], v[114:115], v[30:31], v[12:13] op_sel:[0,1,0]
	v_pk_fma_f32 v[6:7], v[112:113], v[92:93], v[6:7] op_sel:[0,1,0]
	v_pk_fma_f32 v[8:9], v[114:115], v[92:93], v[8:9] op_sel:[0,1,0]
	v_pk_fma_f32 v[2:3], v[112:113], v[96:97], v[2:3] op_sel:[0,1,0]
	v_pk_fma_f32 v[4:5], v[114:115], v[96:97], v[4:5] op_sel:[0,1,0]
	global_load_dwordx4 v[112:115], v106, s[48:49] nt
	s_add_u32 s48, s48, 0xc000
	s_addc_u32 s49, s49, 0
	s_waitcnt vmcnt(31)
	v_pk_fma_f32 v[18:19], v[116:117], v[24:25], v[18:19] op_sel_hi:[1,0,1]
	v_pk_fma_f32 v[20:21], v[118:119], v[24:25], v[20:21] op_sel_hi:[1,0,1]
	v_pk_fma_f32 v[14:15], v[116:117], v[28:29], v[14:15] op_sel_hi:[1,0,1]
	v_pk_fma_f32 v[16:17], v[118:119], v[28:29], v[16:17] op_sel_hi:[1,0,1]
	v_pk_fma_f32 v[10:11], v[116:117], v[32:33], v[10:11] op_sel_hi:[1,0,1]
	v_pk_fma_f32 v[12:13], v[118:119], v[32:33], v[12:13] op_sel_hi:[1,0,1]
	v_pk_fma_f32 v[6:7], v[116:117], v[94:95], v[6:7] op_sel_hi:[1,0,1]
	v_pk_fma_f32 v[8:9], v[118:119], v[94:95], v[8:9] op_sel_hi:[1,0,1]
	v_pk_fma_f32 v[2:3], v[116:117], v[98:99], v[2:3] op_sel_hi:[1,0,1]
	v_pk_fma_f32 v[4:5], v[118:119], v[98:99], v[4:5] op_sel_hi:[1,0,1]
	global_load_dwordx4 v[116:119], v106, s[48:49] nt
	s_add_u32 s48, s48, 0xc000
	s_addc_u32 s49, s49, 0
	s_waitcnt vmcnt(31)
	v_pk_fma_f32 v[18:19], v[120:121], v[24:25], v[18:19] op_sel:[0,1,0]
	v_pk_fma_f32 v[20:21], v[122:123], v[24:25], v[20:21] op_sel:[0,1,0]
	v_pk_fma_f32 v[14:15], v[120:121], v[28:29], v[14:15] op_sel:[0,1,0]
	v_pk_fma_f32 v[16:17], v[122:123], v[28:29], v[16:17] op_sel:[0,1,0]
	v_pk_fma_f32 v[10:11], v[120:121], v[32:33], v[10:11] op_sel:[0,1,0]
	v_pk_fma_f32 v[12:13], v[122:123], v[32:33], v[12:13] op_sel:[0,1,0]
	v_pk_fma_f32 v[6:7], v[120:121], v[94:95], v[6:7] op_sel:[0,1,0]
	v_pk_fma_f32 v[8:9], v[122:123], v[94:95], v[8:9] op_sel:[0,1,0]
	v_pk_fma_f32 v[2:3], v[120:121], v[98:99], v[2:3] op_sel:[0,1,0]
	v_pk_fma_f32 v[4:5], v[122:123], v[98:99], v[4:5] op_sel:[0,1,0]
	global_load_dwordx4 v[120:123], v106, s[48:49] nt
	s_add_u32 s48, s48, 0xc000
	s_addc_u32 s49, s49, 0
	ds_read_b128 v[22:25], v107 offset:32
	ds_read_b128 v[26:29], v107 offset:8224
	ds_read_b128 v[30:33], v107 offset:16416
	ds_read_b128 v[92:95], v107 offset:24608
	ds_read_b128 v[96:99], v107 offset:32800
	s_waitcnt lgkmcnt(5)
	s_waitcnt vmcnt(31)
	v_pk_fma_f32 v[18:19], v[124:125], v[236:237], v[18:19] op_sel_hi:[1,0,1]
	v_pk_fma_f32 v[20:21], v[126:127], v[236:237], v[20:21] op_sel_hi:[1,0,1]
	v_pk_fma_f32 v[14:15], v[124:125], v[240:241], v[14:15] op_sel_hi:[1,0,1]
	v_pk_fma_f32 v[16:17], v[126:127], v[240:241], v[16:17] op_sel_hi:[1,0,1]
	v_pk_fma_f32 v[10:11], v[124:125], v[244:245], v[10:11] op_sel_hi:[1,0,1]
	v_pk_fma_f32 v[12:13], v[126:127], v[244:245], v[12:13] op_sel_hi:[1,0,1]
	v_pk_fma_f32 v[6:7], v[124:125], v[248:249], v[6:7] op_sel_hi:[1,0,1]
	v_pk_fma_f32 v[8:9], v[126:127], v[248:249], v[8:9] op_sel_hi:[1,0,1]
	v_pk_fma_f32 v[2:3], v[124:125], v[100:101], v[2:3] op_sel_hi:[1,0,1]
	v_pk_fma_f32 v[4:5], v[126:127], v[100:101], v[4:5] op_sel_hi:[1,0,1]
	global_load_dwordx4 v[124:127], v106, s[48:49] nt
	s_add_u32 s48, s48, 0xc000
	s_addc_u32 s49, s49, 0
	s_waitcnt vmcnt(31)
	v_pk_fma_f32 v[18:19], v[128:129], v[236:237], v[18:19] op_sel:[0,1,0]
	v_pk_fma_f32 v[20:21], v[130:131], v[236:237], v[20:21] op_sel:[0,1,0]
	v_pk_fma_f32 v[14:15], v[128:129], v[240:241], v[14:15] op_sel:[0,1,0]
	v_pk_fma_f32 v[16:17], v[130:131], v[240:241], v[16:17] op_sel:[0,1,0]
	v_pk_fma_f32 v[10:11], v[128:129], v[244:245], v[10:11] op_sel:[0,1,0]
	v_pk_fma_f32 v[12:13], v[130:131], v[244:245], v[12:13] op_sel:[0,1,0]
	v_pk_fma_f32 v[6:7], v[128:129], v[248:249], v[6:7] op_sel:[0,1,0]
	v_pk_fma_f32 v[8:9], v[130:131], v[248:249], v[8:9] op_sel:[0,1,0]
	v_pk_fma_f32 v[2:3], v[128:129], v[100:101], v[2:3] op_sel:[0,1,0]
	v_pk_fma_f32 v[4:5], v[130:131], v[100:101], v[4:5] op_sel:[0,1,0]
	global_load_dwordx4 v[128:131], v106, s[48:49] nt
	s_add_u32 s48, s48, 0xc000
	s_addc_u32 s49, s49, 0
	s_waitcnt vmcnt(31)
	v_pk_fma_f32 v[18:19], v[132:133], v[238:239], v[18:19] op_sel_hi:[1,0,1]
	v_pk_fma_f32 v[20:21], v[134:135], v[238:239], v[20:21] op_sel_hi:[1,0,1]
	v_pk_fma_f32 v[14:15], v[132:133], v[242:243], v[14:15] op_sel_hi:[1,0,1]
	v_pk_fma_f32 v[16:17], v[134:135], v[242:243], v[16:17] op_sel_hi:[1,0,1]
	v_pk_fma_f32 v[10:11], v[132:133], v[246:247], v[10:11] op_sel_hi:[1,0,1]
	v_pk_fma_f32 v[12:13], v[134:135], v[246:247], v[12:13] op_sel_hi:[1,0,1]
	v_pk_fma_f32 v[6:7], v[132:133], v[250:251], v[6:7] op_sel_hi:[1,0,1]
	v_pk_fma_f32 v[8:9], v[134:135], v[250:251], v[8:9] op_sel_hi:[1,0,1]
	v_pk_fma_f32 v[2:3], v[132:133], v[102:103], v[2:3] op_sel_hi:[1,0,1]
	v_pk_fma_f32 v[4:5], v[134:135], v[102:103], v[4:5] op_sel_hi:[1,0,1]
	global_load_dwordx4 v[132:135], v106, s[48:49] nt
	s_add_u32 s48, s48, 0xc000
	s_addc_u32 s49, s49, 0
	s_waitcnt vmcnt(31)
	v_pk_fma_f32 v[18:19], v[136:137], v[238:239], v[18:19] op_sel:[0,1,0]
	v_pk_fma_f32 v[20:21], v[138:139], v[238:239], v[20:21] op_sel:[0,1,0]
	v_pk_fma_f32 v[14:15], v[136:137], v[242:243], v[14:15] op_sel:[0,1,0]
	v_pk_fma_f32 v[16:17], v[138:139], v[242:243], v[16:17] op_sel:[0,1,0]
	v_pk_fma_f32 v[10:11], v[136:137], v[246:247], v[10:11] op_sel:[0,1,0]
	v_pk_fma_f32 v[12:13], v[138:139], v[246:247], v[12:13] op_sel:[0,1,0]
	v_pk_fma_f32 v[6:7], v[136:137], v[250:251], v[6:7] op_sel:[0,1,0]
	v_pk_fma_f32 v[8:9], v[138:139], v[250:251], v[8:9] op_sel:[0,1,0]
	v_pk_fma_f32 v[2:3], v[136:137], v[102:103], v[2:3] op_sel:[0,1,0]
	v_pk_fma_f32 v[4:5], v[138:139], v[102:103], v[4:5] op_sel:[0,1,0]
	global_load_dwordx4 v[136:139], v106, s[48:49] nt
	s_add_u32 s48, s48, 0xc000
	s_addc_u32 s49, s49, 0
	ds_read_b128 v[236:239], v107 offset:48
	ds_read_b128 v[240:243], v107 offset:8240
	ds_read_b128 v[244:247], v107 offset:16432
	ds_read_b128 v[248:251], v107 offset:24624
	ds_read_b128 v[100:103], v107 offset:32816
	s_waitcnt lgkmcnt(5)
	s_waitcnt vmcnt(31)
	v_pk_fma_f32 v[18:19], v[140:141], v[22:23], v[18:19] op_sel_hi:[1,0,1]
	v_pk_fma_f32 v[20:21], v[142:143], v[22:23], v[20:21] op_sel_hi:[1,0,1]
	v_pk_fma_f32 v[14:15], v[140:141], v[26:27], v[14:15] op_sel_hi:[1,0,1]
	v_pk_fma_f32 v[16:17], v[142:143], v[26:27], v[16:17] op_sel_hi:[1,0,1]
	v_pk_fma_f32 v[10:11], v[140:141], v[30:31], v[10:11] op_sel_hi:[1,0,1]
	v_pk_fma_f32 v[12:13], v[142:143], v[30:31], v[12:13] op_sel_hi:[1,0,1]
	v_pk_fma_f32 v[6:7], v[140:141], v[92:93], v[6:7] op_sel_hi:[1,0,1]
	v_pk_fma_f32 v[8:9], v[142:143], v[92:93], v[8:9] op_sel_hi:[1,0,1]
	v_pk_fma_f32 v[2:3], v[140:141], v[96:97], v[2:3] op_sel_hi:[1,0,1]
	v_pk_fma_f32 v[4:5], v[142:143], v[96:97], v[4:5] op_sel_hi:[1,0,1]
	global_load_dwordx4 v[140:143], v106, s[48:49] nt
	s_add_u32 s48, s48, 0xc000
	s_addc_u32 s49, s49, 0
	s_waitcnt vmcnt(31)
	v_pk_fma_f32 v[18:19], v[144:145], v[22:23], v[18:19] op_sel:[0,1,0]
	v_pk_fma_f32 v[20:21], v[146:147], v[22:23], v[20:21] op_sel:[0,1,0]
	v_pk_fma_f32 v[14:15], v[144:145], v[26:27], v[14:15] op_sel:[0,1,0]
	v_pk_fma_f32 v[16:17], v[146:147], v[26:27], v[16:17] op_sel:[0,1,0]
	v_pk_fma_f32 v[10:11], v[144:145], v[30:31], v[10:11] op_sel:[0,1,0]
	v_pk_fma_f32 v[12:13], v[146:147], v[30:31], v[12:13] op_sel:[0,1,0]
	v_pk_fma_f32 v[6:7], v[144:145], v[92:93], v[6:7] op_sel:[0,1,0]
	v_pk_fma_f32 v[8:9], v[146:147], v[92:93], v[8:9] op_sel:[0,1,0]
	v_pk_fma_f32 v[2:3], v[144:145], v[96:97], v[2:3] op_sel:[0,1,0]
	v_pk_fma_f32 v[4:5], v[146:147], v[96:97], v[4:5] op_sel:[0,1,0]
	global_load_dwordx4 v[144:147], v106, s[48:49] nt
	s_add_u32 s48, s48, 0xc000
	s_addc_u32 s49, s49, 0
	s_waitcnt vmcnt(31)
	v_pk_fma_f32 v[18:19], v[148:149], v[24:25], v[18:19] op_sel_hi:[1,0,1]
	v_pk_fma_f32 v[20:21], v[150:151], v[24:25], v[20:21] op_sel_hi:[1,0,1]
	v_pk_fma_f32 v[14:15], v[148:149], v[28:29], v[14:15] op_sel_hi:[1,0,1]
	v_pk_fma_f32 v[16:17], v[150:151], v[28:29], v[16:17] op_sel_hi:[1,0,1]
	v_pk_fma_f32 v[10:11], v[148:149], v[32:33], v[10:11] op_sel_hi:[1,0,1]
	v_pk_fma_f32 v[12:13], v[150:151], v[32:33], v[12:13] op_sel_hi:[1,0,1]
	v_pk_fma_f32 v[6:7], v[148:149], v[94:95], v[6:7] op_sel_hi:[1,0,1]
	v_pk_fma_f32 v[8:9], v[150:151], v[94:95], v[8:9] op_sel_hi:[1,0,1]
	v_pk_fma_f32 v[2:3], v[148:149], v[98:99], v[2:3] op_sel_hi:[1,0,1]
	v_pk_fma_f32 v[4:5], v[150:151], v[98:99], v[4:5] op_sel_hi:[1,0,1]
	global_load_dwordx4 v[148:151], v106, s[48:49] nt
	s_add_u32 s48, s48, 0xc000
	s_addc_u32 s49, s49, 0
	s_waitcnt vmcnt(31)
	v_pk_fma_f32 v[18:19], v[152:153], v[24:25], v[18:19] op_sel:[0,1,0]
	v_pk_fma_f32 v[20:21], v[154:155], v[24:25], v[20:21] op_sel:[0,1,0]
	v_pk_fma_f32 v[14:15], v[152:153], v[28:29], v[14:15] op_sel:[0,1,0]
	v_pk_fma_f32 v[16:17], v[154:155], v[28:29], v[16:17] op_sel:[0,1,0]
	v_pk_fma_f32 v[10:11], v[152:153], v[32:33], v[10:11] op_sel:[0,1,0]
	v_pk_fma_f32 v[12:13], v[154:155], v[32:33], v[12:13] op_sel:[0,1,0]
	v_pk_fma_f32 v[6:7], v[152:153], v[94:95], v[6:7] op_sel:[0,1,0]
	v_pk_fma_f32 v[8:9], v[154:155], v[94:95], v[8:9] op_sel:[0,1,0]
	v_pk_fma_f32 v[2:3], v[152:153], v[98:99], v[2:3] op_sel:[0,1,0]
	v_pk_fma_f32 v[4:5], v[154:155], v[98:99], v[4:5] op_sel:[0,1,0]
	global_load_dwordx4 v[152:155], v106, s[48:49] nt
	s_add_u32 s48, s48, 0xc000
	s_addc_u32 s49, s49, 0
	ds_read_b128 v[22:25], v107 offset:64
	ds_read_b128 v[26:29], v107 offset:8256
	ds_read_b128 v[30:33], v107 offset:16448
	ds_read_b128 v[92:95], v107 offset:24640
	ds_read_b128 v[96:99], v107 offset:32832
	s_waitcnt lgkmcnt(5)
	s_waitcnt vmcnt(31)
	v_pk_fma_f32 v[18:19], v[156:157], v[236:237], v[18:19] op_sel_hi:[1,0,1]
	v_pk_fma_f32 v[20:21], v[158:159], v[236:237], v[20:21] op_sel_hi:[1,0,1]
	v_pk_fma_f32 v[14:15], v[156:157], v[240:241], v[14:15] op_sel_hi:[1,0,1]
	v_pk_fma_f32 v[16:17], v[158:159], v[240:241], v[16:17] op_sel_hi:[1,0,1]
	v_pk_fma_f32 v[10:11], v[156:157], v[244:245], v[10:11] op_sel_hi:[1,0,1]
	v_pk_fma_f32 v[12:13], v[158:159], v[244:245], v[12:13] op_sel_hi:[1,0,1]
	v_pk_fma_f32 v[6:7], v[156:157], v[248:249], v[6:7] op_sel_hi:[1,0,1]
	v_pk_fma_f32 v[8:9], v[158:159], v[248:249], v[8:9] op_sel_hi:[1,0,1]
	v_pk_fma_f32 v[2:3], v[156:157], v[100:101], v[2:3] op_sel_hi:[1,0,1]
	v_pk_fma_f32 v[4:5], v[158:159], v[100:101], v[4:5] op_sel_hi:[1,0,1]
	global_load_dwordx4 v[156:159], v106, s[48:49] nt
	s_add_u32 s48, s48, 0xc000
	s_addc_u32 s49, s49, 0
	s_waitcnt vmcnt(31)
	v_pk_fma_f32 v[18:19], v[160:161], v[236:237], v[18:19] op_sel:[0,1,0]
	v_pk_fma_f32 v[20:21], v[162:163], v[236:237], v[20:21] op_sel:[0,1,0]
	v_pk_fma_f32 v[14:15], v[160:161], v[240:241], v[14:15] op_sel:[0,1,0]
	v_pk_fma_f32 v[16:17], v[162:163], v[240:241], v[16:17] op_sel:[0,1,0]
	v_pk_fma_f32 v[10:11], v[160:161], v[244:245], v[10:11] op_sel:[0,1,0]
	v_pk_fma_f32 v[12:13], v[162:163], v[244:245], v[12:13] op_sel:[0,1,0]
	v_pk_fma_f32 v[6:7], v[160:161], v[248:249], v[6:7] op_sel:[0,1,0]
	v_pk_fma_f32 v[8:9], v[162:163], v[248:249], v[8:9] op_sel:[0,1,0]
	v_pk_fma_f32 v[2:3], v[160:161], v[100:101], v[2:3] op_sel:[0,1,0]
	v_pk_fma_f32 v[4:5], v[162:163], v[100:101], v[4:5] op_sel:[0,1,0]
	global_load_dwordx4 v[160:163], v106, s[48:49] nt
	s_add_u32 s48, s48, 0xc000
	s_addc_u32 s49, s49, 0
	s_waitcnt vmcnt(31)
	v_pk_fma_f32 v[18:19], v[164:165], v[238:239], v[18:19] op_sel_hi:[1,0,1]
	v_pk_fma_f32 v[20:21], v[166:167], v[238:239], v[20:21] op_sel_hi:[1,0,1]
	v_pk_fma_f32 v[14:15], v[164:165], v[242:243], v[14:15] op_sel_hi:[1,0,1]
	v_pk_fma_f32 v[16:17], v[166:167], v[242:243], v[16:17] op_sel_hi:[1,0,1]
	v_pk_fma_f32 v[10:11], v[164:165], v[246:247], v[10:11] op_sel_hi:[1,0,1]
	v_pk_fma_f32 v[12:13], v[166:167], v[246:247], v[12:13] op_sel_hi:[1,0,1]
	v_pk_fma_f32 v[6:7], v[164:165], v[250:251], v[6:7] op_sel_hi:[1,0,1]
	v_pk_fma_f32 v[8:9], v[166:167], v[250:251], v[8:9] op_sel_hi:[1,0,1]
	v_pk_fma_f32 v[2:3], v[164:165], v[102:103], v[2:3] op_sel_hi:[1,0,1]
	v_pk_fma_f32 v[4:5], v[166:167], v[102:103], v[4:5] op_sel_hi:[1,0,1]
	global_load_dwordx4 v[164:167], v106, s[48:49] nt
	s_add_u32 s48, s48, 0xc000
	s_addc_u32 s49, s49, 0
	s_waitcnt vmcnt(31)
	v_pk_fma_f32 v[18:19], v[168:169], v[238:239], v[18:19] op_sel:[0,1,0]
	v_pk_fma_f32 v[20:21], v[170:171], v[238:239], v[20:21] op_sel:[0,1,0]
	v_pk_fma_f32 v[14:15], v[168:169], v[242:243], v[14:15] op_sel:[0,1,0]
	v_pk_fma_f32 v[16:17], v[170:171], v[242:243], v[16:17] op_sel:[0,1,0]
	v_pk_fma_f32 v[10:11], v[168:169], v[246:247], v[10:11] op_sel:[0,1,0]
	v_pk_fma_f32 v[12:13], v[170:171], v[246:247], v[12:13] op_sel:[0,1,0]
	v_pk_fma_f32 v[6:7], v[168:169], v[250:251], v[6:7] op_sel:[0,1,0]
	v_pk_fma_f32 v[8:9], v[170:171], v[250:251], v[8:9] op_sel:[0,1,0]
	v_pk_fma_f32 v[2:3], v[168:169], v[102:103], v[2:3] op_sel:[0,1,0]
	v_pk_fma_f32 v[4:5], v[170:171], v[102:103], v[4:5] op_sel:[0,1,0]
	global_load_dwordx4 v[168:171], v106, s[48:49] nt
	s_add_u32 s48, s48, 0xc000
	s_addc_u32 s49, s49, 0
	ds_read_b128 v[236:239], v107 offset:80
	ds_read_b128 v[240:243], v107 offset:8272
	ds_read_b128 v[244:247], v107 offset:16464
	ds_read_b128 v[248:251], v107 offset:24656
	ds_read_b128 v[100:103], v107 offset:32848
	s_waitcnt lgkmcnt(5)
	s_waitcnt vmcnt(31)
	v_pk_fma_f32 v[18:19], v[172:173], v[22:23], v[18:19] op_sel_hi:[1,0,1]
	v_pk_fma_f32 v[20:21], v[174:175], v[22:23], v[20:21] op_sel_hi:[1,0,1]
	v_pk_fma_f32 v[14:15], v[172:173], v[26:27], v[14:15] op_sel_hi:[1,0,1]
	v_pk_fma_f32 v[16:17], v[174:175], v[26:27], v[16:17] op_sel_hi:[1,0,1]
	v_pk_fma_f32 v[10:11], v[172:173], v[30:31], v[10:11] op_sel_hi:[1,0,1]
	v_pk_fma_f32 v[12:13], v[174:175], v[30:31], v[12:13] op_sel_hi:[1,0,1]
	v_pk_fma_f32 v[6:7], v[172:173], v[92:93], v[6:7] op_sel_hi:[1,0,1]
	v_pk_fma_f32 v[8:9], v[174:175], v[92:93], v[8:9] op_sel_hi:[1,0,1]
	v_pk_fma_f32 v[2:3], v[172:173], v[96:97], v[2:3] op_sel_hi:[1,0,1]
	v_pk_fma_f32 v[4:5], v[174:175], v[96:97], v[4:5] op_sel_hi:[1,0,1]
	global_load_dwordx4 v[172:175], v106, s[48:49] nt
	s_add_u32 s48, s48, 0xc000
	s_addc_u32 s49, s49, 0
	s_waitcnt vmcnt(31)
	v_pk_fma_f32 v[18:19], v[176:177], v[22:23], v[18:19] op_sel:[0,1,0]
	v_pk_fma_f32 v[20:21], v[178:179], v[22:23], v[20:21] op_sel:[0,1,0]
	v_pk_fma_f32 v[14:15], v[176:177], v[26:27], v[14:15] op_sel:[0,1,0]
	v_pk_fma_f32 v[16:17], v[178:179], v[26:27], v[16:17] op_sel:[0,1,0]
	v_pk_fma_f32 v[10:11], v[176:177], v[30:31], v[10:11] op_sel:[0,1,0]
	v_pk_fma_f32 v[12:13], v[178:179], v[30:31], v[12:13] op_sel:[0,1,0]
	v_pk_fma_f32 v[6:7], v[176:177], v[92:93], v[6:7] op_sel:[0,1,0]
	v_pk_fma_f32 v[8:9], v[178:179], v[92:93], v[8:9] op_sel:[0,1,0]
	v_pk_fma_f32 v[2:3], v[176:177], v[96:97], v[2:3] op_sel:[0,1,0]
	v_pk_fma_f32 v[4:5], v[178:179], v[96:97], v[4:5] op_sel:[0,1,0]
	global_load_dwordx4 v[176:179], v106, s[48:49] nt
	s_add_u32 s48, s48, 0xc000
	s_addc_u32 s49, s49, 0
	s_waitcnt vmcnt(31)
	v_pk_fma_f32 v[18:19], v[180:181], v[24:25], v[18:19] op_sel_hi:[1,0,1]
	v_pk_fma_f32 v[20:21], v[182:183], v[24:25], v[20:21] op_sel_hi:[1,0,1]
	v_pk_fma_f32 v[14:15], v[180:181], v[28:29], v[14:15] op_sel_hi:[1,0,1]
	v_pk_fma_f32 v[16:17], v[182:183], v[28:29], v[16:17] op_sel_hi:[1,0,1]
	v_pk_fma_f32 v[10:11], v[180:181], v[32:33], v[10:11] op_sel_hi:[1,0,1]
	v_pk_fma_f32 v[12:13], v[182:183], v[32:33], v[12:13] op_sel_hi:[1,0,1]
	v_pk_fma_f32 v[6:7], v[180:181], v[94:95], v[6:7] op_sel_hi:[1,0,1]
	v_pk_fma_f32 v[8:9], v[182:183], v[94:95], v[8:9] op_sel_hi:[1,0,1]
	v_pk_fma_f32 v[2:3], v[180:181], v[98:99], v[2:3] op_sel_hi:[1,0,1]
	v_pk_fma_f32 v[4:5], v[182:183], v[98:99], v[4:5] op_sel_hi:[1,0,1]
	global_load_dwordx4 v[180:183], v106, s[48:49] nt
	s_add_u32 s48, s48, 0xc000
	s_addc_u32 s49, s49, 0
	s_waitcnt vmcnt(31)
	v_pk_fma_f32 v[18:19], v[184:185], v[24:25], v[18:19] op_sel:[0,1,0]
	v_pk_fma_f32 v[20:21], v[186:187], v[24:25], v[20:21] op_sel:[0,1,0]
	v_pk_fma_f32 v[14:15], v[184:185], v[28:29], v[14:15] op_sel:[0,1,0]
	v_pk_fma_f32 v[16:17], v[186:187], v[28:29], v[16:17] op_sel:[0,1,0]
	v_pk_fma_f32 v[10:11], v[184:185], v[32:33], v[10:11] op_sel:[0,1,0]
	v_pk_fma_f32 v[12:13], v[186:187], v[32:33], v[12:13] op_sel:[0,1,0]
	v_pk_fma_f32 v[6:7], v[184:185], v[94:95], v[6:7] op_sel:[0,1,0]
	v_pk_fma_f32 v[8:9], v[186:187], v[94:95], v[8:9] op_sel:[0,1,0]
	v_pk_fma_f32 v[2:3], v[184:185], v[98:99], v[2:3] op_sel:[0,1,0]
	v_pk_fma_f32 v[4:5], v[186:187], v[98:99], v[4:5] op_sel:[0,1,0]
	global_load_dwordx4 v[184:187], v106, s[48:49] nt
	s_add_u32 s48, s48, 0xc000
	s_addc_u32 s49, s49, 0
	ds_read_b128 v[22:25], v107 offset:96
	ds_read_b128 v[26:29], v107 offset:8288
	ds_read_b128 v[30:33], v107 offset:16480
	ds_read_b128 v[92:95], v107 offset:24672
	ds_read_b128 v[96:99], v107 offset:32864
	s_waitcnt lgkmcnt(5)
	s_waitcnt vmcnt(31)
	v_pk_fma_f32 v[18:19], v[188:189], v[236:237], v[18:19] op_sel_hi:[1,0,1]
	v_pk_fma_f32 v[20:21], v[190:191], v[236:237], v[20:21] op_sel_hi:[1,0,1]
	v_pk_fma_f32 v[14:15], v[188:189], v[240:241], v[14:15] op_sel_hi:[1,0,1]
	v_pk_fma_f32 v[16:17], v[190:191], v[240:241], v[16:17] op_sel_hi:[1,0,1]
	v_pk_fma_f32 v[10:11], v[188:189], v[244:245], v[10:11] op_sel_hi:[1,0,1]
	v_pk_fma_f32 v[12:13], v[190:191], v[244:245], v[12:13] op_sel_hi:[1,0,1]
	v_pk_fma_f32 v[6:7], v[188:189], v[248:249], v[6:7] op_sel_hi:[1,0,1]
	v_pk_fma_f32 v[8:9], v[190:191], v[248:249], v[8:9] op_sel_hi:[1,0,1]
	v_pk_fma_f32 v[2:3], v[188:189], v[100:101], v[2:3] op_sel_hi:[1,0,1]
	v_pk_fma_f32 v[4:5], v[190:191], v[100:101], v[4:5] op_sel_hi:[1,0,1]
	global_load_dwordx4 v[188:191], v106, s[48:49] nt
	s_add_u32 s48, s48, 0xc000
	s_addc_u32 s49, s49, 0
	s_waitcnt vmcnt(31)
	v_pk_fma_f32 v[18:19], v[192:193], v[236:237], v[18:19] op_sel:[0,1,0]
	v_pk_fma_f32 v[20:21], v[194:195], v[236:237], v[20:21] op_sel:[0,1,0]
	v_pk_fma_f32 v[14:15], v[192:193], v[240:241], v[14:15] op_sel:[0,1,0]
	v_pk_fma_f32 v[16:17], v[194:195], v[240:241], v[16:17] op_sel:[0,1,0]
	v_pk_fma_f32 v[10:11], v[192:193], v[244:245], v[10:11] op_sel:[0,1,0]
	v_pk_fma_f32 v[12:13], v[194:195], v[244:245], v[12:13] op_sel:[0,1,0]
	v_pk_fma_f32 v[6:7], v[192:193], v[248:249], v[6:7] op_sel:[0,1,0]
	v_pk_fma_f32 v[8:9], v[194:195], v[248:249], v[8:9] op_sel:[0,1,0]
	v_pk_fma_f32 v[2:3], v[192:193], v[100:101], v[2:3] op_sel:[0,1,0]
	v_pk_fma_f32 v[4:5], v[194:195], v[100:101], v[4:5] op_sel:[0,1,0]
	global_load_dwordx4 v[192:195], v106, s[48:49] nt
	s_add_u32 s48, s48, 0xc000
	s_addc_u32 s49, s49, 0
	s_waitcnt vmcnt(31)
	v_pk_fma_f32 v[18:19], v[196:197], v[238:239], v[18:19] op_sel_hi:[1,0,1]
	v_pk_fma_f32 v[20:21], v[198:199], v[238:239], v[20:21] op_sel_hi:[1,0,1]
	v_pk_fma_f32 v[14:15], v[196:197], v[242:243], v[14:15] op_sel_hi:[1,0,1]
	v_pk_fma_f32 v[16:17], v[198:199], v[242:243], v[16:17] op_sel_hi:[1,0,1]
	v_pk_fma_f32 v[10:11], v[196:197], v[246:247], v[10:11] op_sel_hi:[1,0,1]
	v_pk_fma_f32 v[12:13], v[198:199], v[246:247], v[12:13] op_sel_hi:[1,0,1]
	v_pk_fma_f32 v[6:7], v[196:197], v[250:251], v[6:7] op_sel_hi:[1,0,1]
	v_pk_fma_f32 v[8:9], v[198:199], v[250:251], v[8:9] op_sel_hi:[1,0,1]
	v_pk_fma_f32 v[2:3], v[196:197], v[102:103], v[2:3] op_sel_hi:[1,0,1]
	v_pk_fma_f32 v[4:5], v[198:199], v[102:103], v[4:5] op_sel_hi:[1,0,1]
	global_load_dwordx4 v[196:199], v106, s[48:49] nt
	s_add_u32 s48, s48, 0xc000
	s_addc_u32 s49, s49, 0
	s_waitcnt vmcnt(31)
	v_pk_fma_f32 v[18:19], v[200:201], v[238:239], v[18:19] op_sel:[0,1,0]
	v_pk_fma_f32 v[20:21], v[202:203], v[238:239], v[20:21] op_sel:[0,1,0]
	v_pk_fma_f32 v[14:15], v[200:201], v[242:243], v[14:15] op_sel:[0,1,0]
	v_pk_fma_f32 v[16:17], v[202:203], v[242:243], v[16:17] op_sel:[0,1,0]
	v_pk_fma_f32 v[10:11], v[200:201], v[246:247], v[10:11] op_sel:[0,1,0]
	v_pk_fma_f32 v[12:13], v[202:203], v[246:247], v[12:13] op_sel:[0,1,0]
	v_pk_fma_f32 v[6:7], v[200:201], v[250:251], v[6:7] op_sel:[0,1,0]
	v_pk_fma_f32 v[8:9], v[202:203], v[250:251], v[8:9] op_sel:[0,1,0]
	v_pk_fma_f32 v[2:3], v[200:201], v[102:103], v[2:3] op_sel:[0,1,0]
	v_pk_fma_f32 v[4:5], v[202:203], v[102:103], v[4:5] op_sel:[0,1,0]
	global_load_dwordx4 v[200:203], v106, s[48:49] nt
	s_add_u32 s48, s48, 0xc000
	s_addc_u32 s49, s49, 0
	ds_read_b128 v[236:239], v107 offset:112
	ds_read_b128 v[240:243], v107 offset:8304
	ds_read_b128 v[244:247], v107 offset:16496
	ds_read_b128 v[248:251], v107 offset:24688
	ds_read_b128 v[100:103], v107 offset:32880
	s_waitcnt lgkmcnt(5)
	s_waitcnt vmcnt(31)
	v_pk_fma_f32 v[18:19], v[204:205], v[22:23], v[18:19] op_sel_hi:[1,0,1]
	v_pk_fma_f32 v[20:21], v[206:207], v[22:23], v[20:21] op_sel_hi:[1,0,1]
	v_pk_fma_f32 v[14:15], v[204:205], v[26:27], v[14:15] op_sel_hi:[1,0,1]
	v_pk_fma_f32 v[16:17], v[206:207], v[26:27], v[16:17] op_sel_hi:[1,0,1]
	v_pk_fma_f32 v[10:11], v[204:205], v[30:31], v[10:11] op_sel_hi:[1,0,1]
	v_pk_fma_f32 v[12:13], v[206:207], v[30:31], v[12:13] op_sel_hi:[1,0,1]
	v_pk_fma_f32 v[6:7], v[204:205], v[92:93], v[6:7] op_sel_hi:[1,0,1]
	v_pk_fma_f32 v[8:9], v[206:207], v[92:93], v[8:9] op_sel_hi:[1,0,1]
	v_pk_fma_f32 v[2:3], v[204:205], v[96:97], v[2:3] op_sel_hi:[1,0,1]
	v_pk_fma_f32 v[4:5], v[206:207], v[96:97], v[4:5] op_sel_hi:[1,0,1]
	global_load_dwordx4 v[204:207], v106, s[48:49] nt
	s_add_u32 s48, s48, 0xc000
	s_addc_u32 s49, s49, 0
	s_waitcnt vmcnt(31)
	v_pk_fma_f32 v[18:19], v[208:209], v[22:23], v[18:19] op_sel:[0,1,0]
	v_pk_fma_f32 v[20:21], v[210:211], v[22:23], v[20:21] op_sel:[0,1,0]
	v_pk_fma_f32 v[14:15], v[208:209], v[26:27], v[14:15] op_sel:[0,1,0]
	v_pk_fma_f32 v[16:17], v[210:211], v[26:27], v[16:17] op_sel:[0,1,0]
	v_pk_fma_f32 v[10:11], v[208:209], v[30:31], v[10:11] op_sel:[0,1,0]
	v_pk_fma_f32 v[12:13], v[210:211], v[30:31], v[12:13] op_sel:[0,1,0]
	v_pk_fma_f32 v[6:7], v[208:209], v[92:93], v[6:7] op_sel:[0,1,0]
	v_pk_fma_f32 v[8:9], v[210:211], v[92:93], v[8:9] op_sel:[0,1,0]
	v_pk_fma_f32 v[2:3], v[208:209], v[96:97], v[2:3] op_sel:[0,1,0]
	v_pk_fma_f32 v[4:5], v[210:211], v[96:97], v[4:5] op_sel:[0,1,0]
	global_load_dwordx4 v[208:211], v106, s[48:49] nt
	s_add_u32 s48, s48, 0xc000
	s_addc_u32 s49, s49, 0
	s_waitcnt vmcnt(31)
	v_pk_fma_f32 v[18:19], v[212:213], v[24:25], v[18:19] op_sel_hi:[1,0,1]
	v_pk_fma_f32 v[20:21], v[214:215], v[24:25], v[20:21] op_sel_hi:[1,0,1]
	v_pk_fma_f32 v[14:15], v[212:213], v[28:29], v[14:15] op_sel_hi:[1,0,1]
	v_pk_fma_f32 v[16:17], v[214:215], v[28:29], v[16:17] op_sel_hi:[1,0,1]
	v_pk_fma_f32 v[10:11], v[212:213], v[32:33], v[10:11] op_sel_hi:[1,0,1]
	v_pk_fma_f32 v[12:13], v[214:215], v[32:33], v[12:13] op_sel_hi:[1,0,1]
	v_pk_fma_f32 v[6:7], v[212:213], v[94:95], v[6:7] op_sel_hi:[1,0,1]
	v_pk_fma_f32 v[8:9], v[214:215], v[94:95], v[8:9] op_sel_hi:[1,0,1]
	v_pk_fma_f32 v[2:3], v[212:213], v[98:99], v[2:3] op_sel_hi:[1,0,1]
	v_pk_fma_f32 v[4:5], v[214:215], v[98:99], v[4:5] op_sel_hi:[1,0,1]
	global_load_dwordx4 v[212:215], v106, s[48:49] nt
	s_add_u32 s48, s48, 0xc000
	s_addc_u32 s49, s49, 0
	s_waitcnt vmcnt(31)
	v_pk_fma_f32 v[18:19], v[216:217], v[24:25], v[18:19] op_sel:[0,1,0]
	v_pk_fma_f32 v[20:21], v[218:219], v[24:25], v[20:21] op_sel:[0,1,0]
	v_pk_fma_f32 v[14:15], v[216:217], v[28:29], v[14:15] op_sel:[0,1,0]
	v_pk_fma_f32 v[16:17], v[218:219], v[28:29], v[16:17] op_sel:[0,1,0]
	v_pk_fma_f32 v[10:11], v[216:217], v[32:33], v[10:11] op_sel:[0,1,0]
	v_pk_fma_f32 v[12:13], v[218:219], v[32:33], v[12:13] op_sel:[0,1,0]
	v_pk_fma_f32 v[6:7], v[216:217], v[94:95], v[6:7] op_sel:[0,1,0]
	v_pk_fma_f32 v[8:9], v[218:219], v[94:95], v[8:9] op_sel:[0,1,0]
	v_pk_fma_f32 v[2:3], v[216:217], v[98:99], v[2:3] op_sel:[0,1,0]
	v_pk_fma_f32 v[4:5], v[218:219], v[98:99], v[4:5] op_sel:[0,1,0]
	global_load_dwordx4 v[216:219], v106, s[48:49] nt
	s_add_u32 s48, s48, 0xc000
	s_addc_u32 s49, s49, 0
	ds_read_b128 v[22:25], v107 offset:128
	ds_read_b128 v[26:29], v107 offset:8320
	ds_read_b128 v[30:33], v107 offset:16512
	ds_read_b128 v[92:95], v107 offset:24704
	ds_read_b128 v[96:99], v107 offset:32896
	s_waitcnt lgkmcnt(5)
	s_waitcnt vmcnt(31)
	v_pk_fma_f32 v[18:19], v[220:221], v[236:237], v[18:19] op_sel_hi:[1,0,1]
	v_pk_fma_f32 v[20:21], v[222:223], v[236:237], v[20:21] op_sel_hi:[1,0,1]
	v_pk_fma_f32 v[14:15], v[220:221], v[240:241], v[14:15] op_sel_hi:[1,0,1]
	v_pk_fma_f32 v[16:17], v[222:223], v[240:241], v[16:17] op_sel_hi:[1,0,1]
	v_pk_fma_f32 v[10:11], v[220:221], v[244:245], v[10:11] op_sel_hi:[1,0,1]
	v_pk_fma_f32 v[12:13], v[222:223], v[244:245], v[12:13] op_sel_hi:[1,0,1]
	v_pk_fma_f32 v[6:7], v[220:221], v[248:249], v[6:7] op_sel_hi:[1,0,1]
	v_pk_fma_f32 v[8:9], v[222:223], v[248:249], v[8:9] op_sel_hi:[1,0,1]
	v_pk_fma_f32 v[2:3], v[220:221], v[100:101], v[2:3] op_sel_hi:[1,0,1]
	v_pk_fma_f32 v[4:5], v[222:223], v[100:101], v[4:5] op_sel_hi:[1,0,1]
	global_load_dwordx4 v[220:223], v106, s[48:49] nt
	s_add_u32 s48, s48, 0xc000
	s_addc_u32 s49, s49, 0
	s_waitcnt vmcnt(31)
	v_pk_fma_f32 v[18:19], v[224:225], v[236:237], v[18:19] op_sel:[0,1,0]
	v_pk_fma_f32 v[20:21], v[226:227], v[236:237], v[20:21] op_sel:[0,1,0]
	v_pk_fma_f32 v[14:15], v[224:225], v[240:241], v[14:15] op_sel:[0,1,0]
	v_pk_fma_f32 v[16:17], v[226:227], v[240:241], v[16:17] op_sel:[0,1,0]
	v_pk_fma_f32 v[10:11], v[224:225], v[244:245], v[10:11] op_sel:[0,1,0]
	v_pk_fma_f32 v[12:13], v[226:227], v[244:245], v[12:13] op_sel:[0,1,0]
	v_pk_fma_f32 v[6:7], v[224:225], v[248:249], v[6:7] op_sel:[0,1,0]
	v_pk_fma_f32 v[8:9], v[226:227], v[248:249], v[8:9] op_sel:[0,1,0]
	v_pk_fma_f32 v[2:3], v[224:225], v[100:101], v[2:3] op_sel:[0,1,0]
	v_pk_fma_f32 v[4:5], v[226:227], v[100:101], v[4:5] op_sel:[0,1,0]
	global_load_dwordx4 v[224:227], v106, s[48:49] nt
	s_add_u32 s48, s48, 0xc000
	s_addc_u32 s49, s49, 0
	s_waitcnt vmcnt(31)
	v_pk_fma_f32 v[18:19], v[228:229], v[238:239], v[18:19] op_sel_hi:[1,0,1]
	v_pk_fma_f32 v[20:21], v[230:231], v[238:239], v[20:21] op_sel_hi:[1,0,1]
	v_pk_fma_f32 v[14:15], v[228:229], v[242:243], v[14:15] op_sel_hi:[1,0,1]
	v_pk_fma_f32 v[16:17], v[230:231], v[242:243], v[16:17] op_sel_hi:[1,0,1]
	v_pk_fma_f32 v[10:11], v[228:229], v[246:247], v[10:11] op_sel_hi:[1,0,1]
	v_pk_fma_f32 v[12:13], v[230:231], v[246:247], v[12:13] op_sel_hi:[1,0,1]
	v_pk_fma_f32 v[6:7], v[228:229], v[250:251], v[6:7] op_sel_hi:[1,0,1]
	v_pk_fma_f32 v[8:9], v[230:231], v[250:251], v[8:9] op_sel_hi:[1,0,1]
	v_pk_fma_f32 v[2:3], v[228:229], v[102:103], v[2:3] op_sel_hi:[1,0,1]
	v_pk_fma_f32 v[4:5], v[230:231], v[102:103], v[4:5] op_sel_hi:[1,0,1]
	global_load_dwordx4 v[228:231], v106, s[48:49] nt
	s_add_u32 s48, s48, 0xc000
	s_addc_u32 s49, s49, 0
	s_waitcnt vmcnt(31)
	v_pk_fma_f32 v[18:19], v[232:233], v[238:239], v[18:19] op_sel:[0,1,0]
	v_pk_fma_f32 v[20:21], v[234:235], v[238:239], v[20:21] op_sel:[0,1,0]
	v_pk_fma_f32 v[14:15], v[232:233], v[242:243], v[14:15] op_sel:[0,1,0]
	v_pk_fma_f32 v[16:17], v[234:235], v[242:243], v[16:17] op_sel:[0,1,0]
	v_pk_fma_f32 v[10:11], v[232:233], v[246:247], v[10:11] op_sel:[0,1,0]
	v_pk_fma_f32 v[12:13], v[234:235], v[246:247], v[12:13] op_sel:[0,1,0]
	v_pk_fma_f32 v[6:7], v[232:233], v[250:251], v[6:7] op_sel:[0,1,0]
	v_pk_fma_f32 v[8:9], v[234:235], v[250:251], v[8:9] op_sel:[0,1,0]
	v_pk_fma_f32 v[2:3], v[232:233], v[102:103], v[2:3] op_sel:[0,1,0]
	v_pk_fma_f32 v[4:5], v[234:235], v[102:103], v[4:5] op_sel:[0,1,0]
	global_load_dwordx4 v[232:235], v106, s[48:49] nt
	s_add_u32 s48, s48, 0xc000
	s_addc_u32 s49, s49, 0
	v_add_u32_e32 v107, 0x80, v107
	s_sub_u32 s50, s50, 1
	s_cmp_lg_u32 s50, 0
	s_cbranch_scc1 .Lada_loop
	ds_read_b128 v[236:239], v107 offset:16
	ds_read_b128 v[240:243], v107 offset:8208
	ds_read_b128 v[244:247], v107 offset:16400
	ds_read_b128 v[248:251], v107 offset:24592
	ds_read_b128 v[100:103], v107 offset:32784
	s_waitcnt lgkmcnt(5)
	s_waitcnt vmcnt(31)
	v_pk_fma_f32 v[18:19], v[108:109], v[22:23], v[18:19] op_sel_hi:[1,0,1]
	v_pk_fma_f32 v[20:21], v[110:111], v[22:23], v[20:21] op_sel_hi:[1,0,1]
	v_pk_fma_f32 v[14:15], v[108:109], v[26:27], v[14:15] op_sel_hi:[1,0,1]
	v_pk_fma_f32 v[16:17], v[110:111], v[26:27], v[16:17] op_sel_hi:[1,0,1]
	v_pk_fma_f32 v[10:11], v[108:109], v[30:31], v[10:11] op_sel_hi:[1,0,1]
	v_pk_fma_f32 v[12:13], v[110:111], v[30:31], v[12:13] op_sel_hi:[1,0,1]
	v_pk_fma_f32 v[6:7], v[108:109], v[92:93], v[6:7] op_sel_hi:[1,0,1]
	v_pk_fma_f32 v[8:9], v[110:111], v[92:93], v[8:9] op_sel_hi:[1,0,1]
	v_pk_fma_f32 v[2:3], v[108:109], v[96:97], v[2:3] op_sel_hi:[1,0,1]
	v_pk_fma_f32 v[4:5], v[110:111], v[96:97], v[4:5] op_sel_hi:[1,0,1]
	s_waitcnt vmcnt(30)
	v_pk_fma_f32 v[18:19], v[112:113], v[22:23], v[18:19] op_sel:[0,1,0]
	v_pk_fma_f32 v[20:21], v[114:115], v[22:23], v[20:21] op_sel:[0,1,0]
	v_pk_fma_f32 v[14:15], v[112:113], v[26:27], v[14:15] op_sel:[0,1,0]
	v_pk_fma_f32 v[16:17], v[114:115], v[26:27], v[16:17] op_sel:[0,1,0]
	v_pk_fma_f32 v[10:11], v[112:113], v[30:31], v[10:11] op_sel:[0,1,0]
	v_pk_fma_f32 v[12:13], v[114:115], v[30:31], v[12:13] op_sel:[0,1,0]
	v_pk_fma_f32 v[6:7], v[112:113], v[92:93], v[6:7] op_sel:[0,1,0]
	v_pk_fma_f32 v[8:9], v[114:115], v[92:93], v[8:9] op_sel:[0,1,0]
	v_pk_fma_f32 v[2:3], v[112:113], v[96:97], v[2:3] op_sel:[0,1,0]
	v_pk_fma_f32 v[4:5], v[114:115], v[96:97], v[4:5] op_sel:[0,1,0]
	s_waitcnt vmcnt(29)
	v_pk_fma_f32 v[18:19], v[116:117], v[24:25], v[18:19] op_sel_hi:[1,0,1]
	v_pk_fma_f32 v[20:21], v[118:119], v[24:25], v[20:21] op_sel_hi:[1,0,1]
	v_pk_fma_f32 v[14:15], v[116:117], v[28:29], v[14:15] op_sel_hi:[1,0,1]
	v_pk_fma_f32 v[16:17], v[118:119], v[28:29], v[16:17] op_sel_hi:[1,0,1]
	v_pk_fma_f32 v[10:11], v[116:117], v[32:33], v[10:11] op_sel_hi:[1,0,1]
	v_pk_fma_f32 v[12:13], v[118:119], v[32:33], v[12:13] op_sel_hi:[1,0,1]
	v_pk_fma_f32 v[6:7], v[116:117], v[94:95], v[6:7] op_sel_hi:[1,0,1]
	v_pk_fma_f32 v[8:9], v[118:119], v[94:95], v[8:9] op_sel_hi:[1,0,1]
	v_pk_fma_f32 v[2:3], v[116:117], v[98:99], v[2:3] op_sel_hi:[1,0,1]
	v_pk_fma_f32 v[4:5], v[118:119], v[98:99], v[4:5] op_sel_hi:[1,0,1]
	s_waitcnt vmcnt(28)
	v_pk_fma_f32 v[18:19], v[120:121], v[24:25], v[18:19] op_sel:[0,1,0]
	v_pk_fma_f32 v[20:21], v[122:123], v[24:25], v[20:21] op_sel:[0,1,0]
	v_pk_fma_f32 v[14:15], v[120:121], v[28:29], v[14:15] op_sel:[0,1,0]
	v_pk_fma_f32 v[16:17], v[122:123], v[28:29], v[16:17] op_sel:[0,1,0]
	v_pk_fma_f32 v[10:11], v[120:121], v[32:33], v[10:11] op_sel:[0,1,0]
	v_pk_fma_f32 v[12:13], v[122:123], v[32:33], v[12:13] op_sel:[0,1,0]
	v_pk_fma_f32 v[6:7], v[120:121], v[94:95], v[6:7] op_sel:[0,1,0]
	v_pk_fma_f32 v[8:9], v[122:123], v[94:95], v[8:9] op_sel:[0,1,0]
	v_pk_fma_f32 v[2:3], v[120:121], v[98:99], v[2:3] op_sel:[0,1,0]
	v_pk_fma_f32 v[4:5], v[122:123], v[98:99], v[4:5] op_sel:[0,1,0]
	ds_read_b128 v[22:25], v107 offset:32
	ds_read_b128 v[26:29], v107 offset:8224
	ds_read_b128 v[30:33], v107 offset:16416
	ds_read_b128 v[92:95], v107 offset:24608
	ds_read_b128 v[96:99], v107 offset:32800
	s_waitcnt lgkmcnt(5)
	s_waitcnt vmcnt(27)
	v_pk_fma_f32 v[18:19], v[124:125], v[236:237], v[18:19] op_sel_hi:[1,0,1]
	v_pk_fma_f32 v[20:21], v[126:127], v[236:237], v[20:21] op_sel_hi:[1,0,1]
	v_pk_fma_f32 v[14:15], v[124:125], v[240:241], v[14:15] op_sel_hi:[1,0,1]
	v_pk_fma_f32 v[16:17], v[126:127], v[240:241], v[16:17] op_sel_hi:[1,0,1]
	v_pk_fma_f32 v[10:11], v[124:125], v[244:245], v[10:11] op_sel_hi:[1,0,1]
	v_pk_fma_f32 v[12:13], v[126:127], v[244:245], v[12:13] op_sel_hi:[1,0,1]
	v_pk_fma_f32 v[6:7], v[124:125], v[248:249], v[6:7] op_sel_hi:[1,0,1]
	v_pk_fma_f32 v[8:9], v[126:127], v[248:249], v[8:9] op_sel_hi:[1,0,1]
	v_pk_fma_f32 v[2:3], v[124:125], v[100:101], v[2:3] op_sel_hi:[1,0,1]
	v_pk_fma_f32 v[4:5], v[126:127], v[100:101], v[4:5] op_sel_hi:[1,0,1]
	s_waitcnt vmcnt(26)
	v_pk_fma_f32 v[18:19], v[128:129], v[236:237], v[18:19] op_sel:[0,1,0]
	v_pk_fma_f32 v[20:21], v[130:131], v[236:237], v[20:21] op_sel:[0,1,0]
	v_pk_fma_f32 v[14:15], v[128:129], v[240:241], v[14:15] op_sel:[0,1,0]
	v_pk_fma_f32 v[16:17], v[130:131], v[240:241], v[16:17] op_sel:[0,1,0]
	v_pk_fma_f32 v[10:11], v[128:129], v[244:245], v[10:11] op_sel:[0,1,0]
	v_pk_fma_f32 v[12:13], v[130:131], v[244:245], v[12:13] op_sel:[0,1,0]
	v_pk_fma_f32 v[6:7], v[128:129], v[248:249], v[6:7] op_sel:[0,1,0]
	v_pk_fma_f32 v[8:9], v[130:131], v[248:249], v[8:9] op_sel:[0,1,0]
	v_pk_fma_f32 v[2:3], v[128:129], v[100:101], v[2:3] op_sel:[0,1,0]
	v_pk_fma_f32 v[4:5], v[130:131], v[100:101], v[4:5] op_sel:[0,1,0]
	s_waitcnt vmcnt(25)
	v_pk_fma_f32 v[18:19], v[132:133], v[238:239], v[18:19] op_sel_hi:[1,0,1]
	v_pk_fma_f32 v[20:21], v[134:135], v[238:239], v[20:21] op_sel_hi:[1,0,1]
	v_pk_fma_f32 v[14:15], v[132:133], v[242:243], v[14:15] op_sel_hi:[1,0,1]
	v_pk_fma_f32 v[16:17], v[134:135], v[242:243], v[16:17] op_sel_hi:[1,0,1]
	v_pk_fma_f32 v[10:11], v[132:133], v[246:247], v[10:11] op_sel_hi:[1,0,1]
	v_pk_fma_f32 v[12:13], v[134:135], v[246:247], v[12:13] op_sel_hi:[1,0,1]
	v_pk_fma_f32 v[6:7], v[132:133], v[250:251], v[6:7] op_sel_hi:[1,0,1]
	v_pk_fma_f32 v[8:9], v[134:135], v[250:251], v[8:9] op_sel_hi:[1,0,1]
	v_pk_fma_f32 v[2:3], v[132:133], v[102:103], v[2:3] op_sel_hi:[1,0,1]
	v_pk_fma_f32 v[4:5], v[134:135], v[102:103], v[4:5] op_sel_hi:[1,0,1]
	s_waitcnt vmcnt(24)
	v_pk_fma_f32 v[18:19], v[136:137], v[238:239], v[18:19] op_sel:[0,1,0]
	v_pk_fma_f32 v[20:21], v[138:139], v[238:239], v[20:21] op_sel:[0,1,0]
	v_pk_fma_f32 v[14:15], v[136:137], v[242:243], v[14:15] op_sel:[0,1,0]
	v_pk_fma_f32 v[16:17], v[138:139], v[242:243], v[16:17] op_sel:[0,1,0]
	v_pk_fma_f32 v[10:11], v[136:137], v[246:247], v[10:11] op_sel:[0,1,0]
	v_pk_fma_f32 v[12:13], v[138:139], v[246:247], v[12:13] op_sel:[0,1,0]
	v_pk_fma_f32 v[6:7], v[136:137], v[250:251], v[6:7] op_sel:[0,1,0]
	v_pk_fma_f32 v[8:9], v[138:139], v[250:251], v[8:9] op_sel:[0,1,0]
	v_pk_fma_f32 v[2:3], v[136:137], v[102:103], v[2:3] op_sel:[0,1,0]
	v_pk_fma_f32 v[4:5], v[138:139], v[102:103], v[4:5] op_sel:[0,1,0]
	ds_read_b128 v[236:239], v107 offset:48
	ds_read_b128 v[240:243], v107 offset:8240
	ds_read_b128 v[244:247], v107 offset:16432
	ds_read_b128 v[248:251], v107 offset:24624
	ds_read_b128 v[100:103], v107 offset:32816
	s_waitcnt lgkmcnt(5)
	s_waitcnt vmcnt(23)
	v_pk_fma_f32 v[18:19], v[140:141], v[22:23], v[18:19] op_sel_hi:[1,0,1]
	v_pk_fma_f32 v[20:21], v[142:143], v[22:23], v[20:21] op_sel_hi:[1,0,1]
	v_pk_fma_f32 v[14:15], v[140:141], v[26:27], v[14:15] op_sel_hi:[1,0,1]
	v_pk_fma_f32 v[16:17], v[142:143], v[26:27], v[16:17] op_sel_hi:[1,0,1]
	v_pk_fma_f32 v[10:11], v[140:141], v[30:31], v[10:11] op_sel_hi:[1,0,1]
	v_pk_fma_f32 v[12:13], v[142:143], v[30:31], v[12:13] op_sel_hi:[1,0,1]
	v_pk_fma_f32 v[6:7], v[140:141], v[92:93], v[6:7] op_sel_hi:[1,0,1]
	v_pk_fma_f32 v[8:9], v[142:143], v[92:93], v[8:9] op_sel_hi:[1,0,1]
	v_pk_fma_f32 v[2:3], v[140:141], v[96:97], v[2:3] op_sel_hi:[1,0,1]
	v_pk_fma_f32 v[4:5], v[142:143], v[96:97], v[4:5] op_sel_hi:[1,0,1]
	s_waitcnt vmcnt(22)
	v_pk_fma_f32 v[18:19], v[144:145], v[22:23], v[18:19] op_sel:[0,1,0]
	v_pk_fma_f32 v[20:21], v[146:147], v[22:23], v[20:21] op_sel:[0,1,0]
	v_pk_fma_f32 v[14:15], v[144:145], v[26:27], v[14:15] op_sel:[0,1,0]
	v_pk_fma_f32 v[16:17], v[146:147], v[26:27], v[16:17] op_sel:[0,1,0]
	v_pk_fma_f32 v[10:11], v[144:145], v[30:31], v[10:11] op_sel:[0,1,0]
	v_pk_fma_f32 v[12:13], v[146:147], v[30:31], v[12:13] op_sel:[0,1,0]
	v_pk_fma_f32 v[6:7], v[144:145], v[92:93], v[6:7] op_sel:[0,1,0]
	v_pk_fma_f32 v[8:9], v[146:147], v[92:93], v[8:9] op_sel:[0,1,0]
	v_pk_fma_f32 v[2:3], v[144:145], v[96:97], v[2:3] op_sel:[0,1,0]
	v_pk_fma_f32 v[4:5], v[146:147], v[96:97], v[4:5] op_sel:[0,1,0]
	s_waitcnt vmcnt(21)
	v_pk_fma_f32 v[18:19], v[148:149], v[24:25], v[18:19] op_sel_hi:[1,0,1]
	v_pk_fma_f32 v[20:21], v[150:151], v[24:25], v[20:21] op_sel_hi:[1,0,1]
	v_pk_fma_f32 v[14:15], v[148:149], v[28:29], v[14:15] op_sel_hi:[1,0,1]
	v_pk_fma_f32 v[16:17], v[150:151], v[28:29], v[16:17] op_sel_hi:[1,0,1]
	v_pk_fma_f32 v[10:11], v[148:149], v[32:33], v[10:11] op_sel_hi:[1,0,1]
	v_pk_fma_f32 v[12:13], v[150:151], v[32:33], v[12:13] op_sel_hi:[1,0,1]
	v_pk_fma_f32 v[6:7], v[148:149], v[94:95], v[6:7] op_sel_hi:[1,0,1]
	v_pk_fma_f32 v[8:9], v[150:151], v[94:95], v[8:9] op_sel_hi:[1,0,1]
	v_pk_fma_f32 v[2:3], v[148:149], v[98:99], v[2:3] op_sel_hi:[1,0,1]
	v_pk_fma_f32 v[4:5], v[150:151], v[98:99], v[4:5] op_sel_hi:[1,0,1]
	s_waitcnt vmcnt(20)
	v_pk_fma_f32 v[18:19], v[152:153], v[24:25], v[18:19] op_sel:[0,1,0]
	v_pk_fma_f32 v[20:21], v[154:155], v[24:25], v[20:21] op_sel:[0,1,0]
	v_pk_fma_f32 v[14:15], v[152:153], v[28:29], v[14:15] op_sel:[0,1,0]
	v_pk_fma_f32 v[16:17], v[154:155], v[28:29], v[16:17] op_sel:[0,1,0]
	v_pk_fma_f32 v[10:11], v[152:153], v[32:33], v[10:11] op_sel:[0,1,0]
	v_pk_fma_f32 v[12:13], v[154:155], v[32:33], v[12:13] op_sel:[0,1,0]
	v_pk_fma_f32 v[6:7], v[152:153], v[94:95], v[6:7] op_sel:[0,1,0]
	v_pk_fma_f32 v[8:9], v[154:155], v[94:95], v[8:9] op_sel:[0,1,0]
	v_pk_fma_f32 v[2:3], v[152:153], v[98:99], v[2:3] op_sel:[0,1,0]
	v_pk_fma_f32 v[4:5], v[154:155], v[98:99], v[4:5] op_sel:[0,1,0]
	ds_read_b128 v[22:25], v107 offset:64
	ds_read_b128 v[26:29], v107 offset:8256
	ds_read_b128 v[30:33], v107 offset:16448
	ds_read_b128 v[92:95], v107 offset:24640
	ds_read_b128 v[96:99], v107 offset:32832
	s_waitcnt lgkmcnt(5)
	s_waitcnt vmcnt(19)
	v_pk_fma_f32 v[18:19], v[156:157], v[236:237], v[18:19] op_sel_hi:[1,0,1]
	v_pk_fma_f32 v[20:21], v[158:159], v[236:237], v[20:21] op_sel_hi:[1,0,1]
	v_pk_fma_f32 v[14:15], v[156:157], v[240:241], v[14:15] op_sel_hi:[1,0,1]
	v_pk_fma_f32 v[16:17], v[158:159], v[240:241], v[16:17] op_sel_hi:[1,0,1]
	v_pk_fma_f32 v[10:11], v[156:157], v[244:245], v[10:11] op_sel_hi:[1,0,1]
	v_pk_fma_f32 v[12:13], v[158:159], v[244:245], v[12:13] op_sel_hi:[1,0,1]
	v_pk_fma_f32 v[6:7], v[156:157], v[248:249], v[6:7] op_sel_hi:[1,0,1]
	v_pk_fma_f32 v[8:9], v[158:159], v[248:249], v[8:9] op_sel_hi:[1,0,1]
	v_pk_fma_f32 v[2:3], v[156:157], v[100:101], v[2:3] op_sel_hi:[1,0,1]
	v_pk_fma_f32 v[4:5], v[158:159], v[100:101], v[4:5] op_sel_hi:[1,0,1]
	s_waitcnt vmcnt(18)
	v_pk_fma_f32 v[18:19], v[160:161], v[236:237], v[18:19] op_sel:[0,1,0]
	v_pk_fma_f32 v[20:21], v[162:163], v[236:237], v[20:21] op_sel:[0,1,0]
	v_pk_fma_f32 v[14:15], v[160:161], v[240:241], v[14:15] op_sel:[0,1,0]
	v_pk_fma_f32 v[16:17], v[162:163], v[240:241], v[16:17] op_sel:[0,1,0]
	v_pk_fma_f32 v[10:11], v[160:161], v[244:245], v[10:11] op_sel:[0,1,0]
	v_pk_fma_f32 v[12:13], v[162:163], v[244:245], v[12:13] op_sel:[0,1,0]
	v_pk_fma_f32 v[6:7], v[160:161], v[248:249], v[6:7] op_sel:[0,1,0]
	v_pk_fma_f32 v[8:9], v[162:163], v[248:249], v[8:9] op_sel:[0,1,0]
	v_pk_fma_f32 v[2:3], v[160:161], v[100:101], v[2:3] op_sel:[0,1,0]
	v_pk_fma_f32 v[4:5], v[162:163], v[100:101], v[4:5] op_sel:[0,1,0]
	s_waitcnt vmcnt(17)
	v_pk_fma_f32 v[18:19], v[164:165], v[238:239], v[18:19] op_sel_hi:[1,0,1]
	v_pk_fma_f32 v[20:21], v[166:167], v[238:239], v[20:21] op_sel_hi:[1,0,1]
	v_pk_fma_f32 v[14:15], v[164:165], v[242:243], v[14:15] op_sel_hi:[1,0,1]
	v_pk_fma_f32 v[16:17], v[166:167], v[242:243], v[16:17] op_sel_hi:[1,0,1]
	v_pk_fma_f32 v[10:11], v[164:165], v[246:247], v[10:11] op_sel_hi:[1,0,1]
	v_pk_fma_f32 v[12:13], v[166:167], v[246:247], v[12:13] op_sel_hi:[1,0,1]
	v_pk_fma_f32 v[6:7], v[164:165], v[250:251], v[6:7] op_sel_hi:[1,0,1]
	v_pk_fma_f32 v[8:9], v[166:167], v[250:251], v[8:9] op_sel_hi:[1,0,1]
	v_pk_fma_f32 v[2:3], v[164:165], v[102:103], v[2:3] op_sel_hi:[1,0,1]
	v_pk_fma_f32 v[4:5], v[166:167], v[102:103], v[4:5] op_sel_hi:[1,0,1]
	s_waitcnt vmcnt(16)
	v_pk_fma_f32 v[18:19], v[168:169], v[238:239], v[18:19] op_sel:[0,1,0]
	v_pk_fma_f32 v[20:21], v[170:171], v[238:239], v[20:21] op_sel:[0,1,0]
	v_pk_fma_f32 v[14:15], v[168:169], v[242:243], v[14:15] op_sel:[0,1,0]
	v_pk_fma_f32 v[16:17], v[170:171], v[242:243], v[16:17] op_sel:[0,1,0]
	v_pk_fma_f32 v[10:11], v[168:169], v[246:247], v[10:11] op_sel:[0,1,0]
	v_pk_fma_f32 v[12:13], v[170:171], v[246:247], v[12:13] op_sel:[0,1,0]
	v_pk_fma_f32 v[6:7], v[168:169], v[250:251], v[6:7] op_sel:[0,1,0]
	v_pk_fma_f32 v[8:9], v[170:171], v[250:251], v[8:9] op_sel:[0,1,0]
	v_pk_fma_f32 v[2:3], v[168:169], v[102:103], v[2:3] op_sel:[0,1,0]
	v_pk_fma_f32 v[4:5], v[170:171], v[102:103], v[4:5] op_sel:[0,1,0]
	ds_read_b128 v[236:239], v107 offset:80
	ds_read_b128 v[240:243], v107 offset:8272
	ds_read_b128 v[244:247], v107 offset:16464
	ds_read_b128 v[248:251], v107 offset:24656
	ds_read_b128 v[100:103], v107 offset:32848
	s_waitcnt lgkmcnt(5)
	s_waitcnt vmcnt(15)
	v_pk_fma_f32 v[18:19], v[172:173], v[22:23], v[18:19] op_sel_hi:[1,0,1]
	v_pk_fma_f32 v[20:21], v[174:175], v[22:23], v[20:21] op_sel_hi:[1,0,1]
	v_pk_fma_f32 v[14:15], v[172:173], v[26:27], v[14:15] op_sel_hi:[1,0,1]
	v_pk_fma_f32 v[16:17], v[174:175], v[26:27], v[16:17] op_sel_hi:[1,0,1]
	v_pk_fma_f32 v[10:11], v[172:173], v[30:31], v[10:11] op_sel_hi:[1,0,1]
	v_pk_fma_f32 v[12:13], v[174:175], v[30:31], v[12:13] op_sel_hi:[1,0,1]
	v_pk_fma_f32 v[6:7], v[172:173], v[92:93], v[6:7] op_sel_hi:[1,0,1]
	v_pk_fma_f32 v[8:9], v[174:175], v[92:93], v[8:9] op_sel_hi:[1,0,1]
	v_pk_fma_f32 v[2:3], v[172:173], v[96:97], v[2:3] op_sel_hi:[1,0,1]
	v_pk_fma_f32 v[4:5], v[174:175], v[96:97], v[4:5] op_sel_hi:[1,0,1]
	s_waitcnt vmcnt(14)
	v_pk_fma_f32 v[18:19], v[176:177], v[22:23], v[18:19] op_sel:[0,1,0]
	v_pk_fma_f32 v[20:21], v[178:179], v[22:23], v[20:21] op_sel:[0,1,0]
	v_pk_fma_f32 v[14:15], v[176:177], v[26:27], v[14:15] op_sel:[0,1,0]
	v_pk_fma_f32 v[16:17], v[178:179], v[26:27], v[16:17] op_sel:[0,1,0]
	v_pk_fma_f32 v[10:11], v[176:177], v[30:31], v[10:11] op_sel:[0,1,0]
	v_pk_fma_f32 v[12:13], v[178:179], v[30:31], v[12:13] op_sel:[0,1,0]
	v_pk_fma_f32 v[6:7], v[176:177], v[92:93], v[6:7] op_sel:[0,1,0]
	v_pk_fma_f32 v[8:9], v[178:179], v[92:93], v[8:9] op_sel:[0,1,0]
	v_pk_fma_f32 v[2:3], v[176:177], v[96:97], v[2:3] op_sel:[0,1,0]
	v_pk_fma_f32 v[4:5], v[178:179], v[96:97], v[4:5] op_sel:[0,1,0]
	s_waitcnt vmcnt(13)
	v_pk_fma_f32 v[18:19], v[180:181], v[24:25], v[18:19] op_sel_hi:[1,0,1]
	v_pk_fma_f32 v[20:21], v[182:183], v[24:25], v[20:21] op_sel_hi:[1,0,1]
	v_pk_fma_f32 v[14:15], v[180:181], v[28:29], v[14:15] op_sel_hi:[1,0,1]
	v_pk_fma_f32 v[16:17], v[182:183], v[28:29], v[16:17] op_sel_hi:[1,0,1]
	v_pk_fma_f32 v[10:11], v[180:181], v[32:33], v[10:11] op_sel_hi:[1,0,1]
	v_pk_fma_f32 v[12:13], v[182:183], v[32:33], v[12:13] op_sel_hi:[1,0,1]
	v_pk_fma_f32 v[6:7], v[180:181], v[94:95], v[6:7] op_sel_hi:[1,0,1]
	v_pk_fma_f32 v[8:9], v[182:183], v[94:95], v[8:9] op_sel_hi:[1,0,1]
	v_pk_fma_f32 v[2:3], v[180:181], v[98:99], v[2:3] op_sel_hi:[1,0,1]
	v_pk_fma_f32 v[4:5], v[182:183], v[98:99], v[4:5] op_sel_hi:[1,0,1]
	s_waitcnt vmcnt(12)
	v_pk_fma_f32 v[18:19], v[184:185], v[24:25], v[18:19] op_sel:[0,1,0]
	v_pk_fma_f32 v[20:21], v[186:187], v[24:25], v[20:21] op_sel:[0,1,0]
	v_pk_fma_f32 v[14:15], v[184:185], v[28:29], v[14:15] op_sel:[0,1,0]
	v_pk_fma_f32 v[16:17], v[186:187], v[28:29], v[16:17] op_sel:[0,1,0]
	v_pk_fma_f32 v[10:11], v[184:185], v[32:33], v[10:11] op_sel:[0,1,0]
	v_pk_fma_f32 v[12:13], v[186:187], v[32:33], v[12:13] op_sel:[0,1,0]
	v_pk_fma_f32 v[6:7], v[184:185], v[94:95], v[6:7] op_sel:[0,1,0]
	v_pk_fma_f32 v[8:9], v[186:187], v[94:95], v[8:9] op_sel:[0,1,0]
	v_pk_fma_f32 v[2:3], v[184:185], v[98:99], v[2:3] op_sel:[0,1,0]
	v_pk_fma_f32 v[4:5], v[186:187], v[98:99], v[4:5] op_sel:[0,1,0]
	ds_read_b128 v[22:25], v107 offset:96
	ds_read_b128 v[26:29], v107 offset:8288
	ds_read_b128 v[30:33], v107 offset:16480
	ds_read_b128 v[92:95], v107 offset:24672
	ds_read_b128 v[96:99], v107 offset:32864
	s_waitcnt lgkmcnt(5)
	s_waitcnt vmcnt(11)
	v_pk_fma_f32 v[18:19], v[188:189], v[236:237], v[18:19] op_sel_hi:[1,0,1]
	v_pk_fma_f32 v[20:21], v[190:191], v[236:237], v[20:21] op_sel_hi:[1,0,1]
	v_pk_fma_f32 v[14:15], v[188:189], v[240:241], v[14:15] op_sel_hi:[1,0,1]
	v_pk_fma_f32 v[16:17], v[190:191], v[240:241], v[16:17] op_sel_hi:[1,0,1]
	v_pk_fma_f32 v[10:11], v[188:189], v[244:245], v[10:11] op_sel_hi:[1,0,1]
	v_pk_fma_f32 v[12:13], v[190:191], v[244:245], v[12:13] op_sel_hi:[1,0,1]
	v_pk_fma_f32 v[6:7], v[188:189], v[248:249], v[6:7] op_sel_hi:[1,0,1]
	v_pk_fma_f32 v[8:9], v[190:191], v[248:249], v[8:9] op_sel_hi:[1,0,1]
	v_pk_fma_f32 v[2:3], v[188:189], v[100:101], v[2:3] op_sel_hi:[1,0,1]
	v_pk_fma_f32 v[4:5], v[190:191], v[100:101], v[4:5] op_sel_hi:[1,0,1]
	s_waitcnt vmcnt(10)
	v_pk_fma_f32 v[18:19], v[192:193], v[236:237], v[18:19] op_sel:[0,1,0]
	v_pk_fma_f32 v[20:21], v[194:195], v[236:237], v[20:21] op_sel:[0,1,0]
	v_pk_fma_f32 v[14:15], v[192:193], v[240:241], v[14:15] op_sel:[0,1,0]
	v_pk_fma_f32 v[16:17], v[194:195], v[240:241], v[16:17] op_sel:[0,1,0]
	v_pk_fma_f32 v[10:11], v[192:193], v[244:245], v[10:11] op_sel:[0,1,0]
	v_pk_fma_f32 v[12:13], v[194:195], v[244:245], v[12:13] op_sel:[0,1,0]
	v_pk_fma_f32 v[6:7], v[192:193], v[248:249], v[6:7] op_sel:[0,1,0]
	v_pk_fma_f32 v[8:9], v[194:195], v[248:249], v[8:9] op_sel:[0,1,0]
	v_pk_fma_f32 v[2:3], v[192:193], v[100:101], v[2:3] op_sel:[0,1,0]
	v_pk_fma_f32 v[4:5], v[194:195], v[100:101], v[4:5] op_sel:[0,1,0]
	s_waitcnt vmcnt(9)
	v_pk_fma_f32 v[18:19], v[196:197], v[238:239], v[18:19] op_sel_hi:[1,0,1]
	v_pk_fma_f32 v[20:21], v[198:199], v[238:239], v[20:21] op_sel_hi:[1,0,1]
	v_pk_fma_f32 v[14:15], v[196:197], v[242:243], v[14:15] op_sel_hi:[1,0,1]
	v_pk_fma_f32 v[16:17], v[198:199], v[242:243], v[16:17] op_sel_hi:[1,0,1]
	v_pk_fma_f32 v[10:11], v[196:197], v[246:247], v[10:11] op_sel_hi:[1,0,1]
	v_pk_fma_f32 v[12:13], v[198:199], v[246:247], v[12:13] op_sel_hi:[1,0,1]
	v_pk_fma_f32 v[6:7], v[196:197], v[250:251], v[6:7] op_sel_hi:[1,0,1]
	v_pk_fma_f32 v[8:9], v[198:199], v[250:251], v[8:9] op_sel_hi:[1,0,1]
	v_pk_fma_f32 v[2:3], v[196:197], v[102:103], v[2:3] op_sel_hi:[1,0,1]
	v_pk_fma_f32 v[4:5], v[198:199], v[102:103], v[4:5] op_sel_hi:[1,0,1]
	s_waitcnt vmcnt(8)
	v_pk_fma_f32 v[18:19], v[200:201], v[238:239], v[18:19] op_sel:[0,1,0]
	v_pk_fma_f32 v[20:21], v[202:203], v[238:239], v[20:21] op_sel:[0,1,0]
	v_pk_fma_f32 v[14:15], v[200:201], v[242:243], v[14:15] op_sel:[0,1,0]
	v_pk_fma_f32 v[16:17], v[202:203], v[242:243], v[16:17] op_sel:[0,1,0]
	v_pk_fma_f32 v[10:11], v[200:201], v[246:247], v[10:11] op_sel:[0,1,0]
	v_pk_fma_f32 v[12:13], v[202:203], v[246:247], v[12:13] op_sel:[0,1,0]
	v_pk_fma_f32 v[6:7], v[200:201], v[250:251], v[6:7] op_sel:[0,1,0]
	v_pk_fma_f32 v[8:9], v[202:203], v[250:251], v[8:9] op_sel:[0,1,0]
	v_pk_fma_f32 v[2:3], v[200:201], v[102:103], v[2:3] op_sel:[0,1,0]
	v_pk_fma_f32 v[4:5], v[202:203], v[102:103], v[4:5] op_sel:[0,1,0]
	ds_read_b128 v[236:239], v107 offset:112
	ds_read_b128 v[240:243], v107 offset:8304
	ds_read_b128 v[244:247], v107 offset:16496
	ds_read_b128 v[248:251], v107 offset:24688
	ds_read_b128 v[100:103], v107 offset:32880
	s_waitcnt lgkmcnt(5)
	s_waitcnt vmcnt(7)
	v_pk_fma_f32 v[18:19], v[204:205], v[22:23], v[18:19] op_sel_hi:[1,0,1]
	v_pk_fma_f32 v[20:21], v[206:207], v[22:23], v[20:21] op_sel_hi:[1,0,1]
	v_pk_fma_f32 v[14:15], v[204:205], v[26:27], v[14:15] op_sel_hi:[1,0,1]
	v_pk_fma_f32 v[16:17], v[206:207], v[26:27], v[16:17] op_sel_hi:[1,0,1]
	v_pk_fma_f32 v[10:11], v[204:205], v[30:31], v[10:11] op_sel_hi:[1,0,1]
	v_pk_fma_f32 v[12:13], v[206:207], v[30:31], v[12:13] op_sel_hi:[1,0,1]
	v_pk_fma_f32 v[6:7], v[204:205], v[92:93], v[6:7] op_sel_hi:[1,0,1]
	v_pk_fma_f32 v[8:9], v[206:207], v[92:93], v[8:9] op_sel_hi:[1,0,1]
	v_pk_fma_f32 v[2:3], v[204:205], v[96:97], v[2:3] op_sel_hi:[1,0,1]
	v_pk_fma_f32 v[4:5], v[206:207], v[96:97], v[4:5] op_sel_hi:[1,0,1]
	s_waitcnt vmcnt(6)
	v_pk_fma_f32 v[18:19], v[208:209], v[22:23], v[18:19] op_sel:[0,1,0]
	v_pk_fma_f32 v[20:21], v[210:211], v[22:23], v[20:21] op_sel:[0,1,0]
	v_pk_fma_f32 v[14:15], v[208:209], v[26:27], v[14:15] op_sel:[0,1,0]
	v_pk_fma_f32 v[16:17], v[210:211], v[26:27], v[16:17] op_sel:[0,1,0]
	v_pk_fma_f32 v[10:11], v[208:209], v[30:31], v[10:11] op_sel:[0,1,0]
	v_pk_fma_f32 v[12:13], v[210:211], v[30:31], v[12:13] op_sel:[0,1,0]
	v_pk_fma_f32 v[6:7], v[208:209], v[92:93], v[6:7] op_sel:[0,1,0]
	v_pk_fma_f32 v[8:9], v[210:211], v[92:93], v[8:9] op_sel:[0,1,0]
	v_pk_fma_f32 v[2:3], v[208:209], v[96:97], v[2:3] op_sel:[0,1,0]
	v_pk_fma_f32 v[4:5], v[210:211], v[96:97], v[4:5] op_sel:[0,1,0]
	s_waitcnt vmcnt(5)
	v_pk_fma_f32 v[18:19], v[212:213], v[24:25], v[18:19] op_sel_hi:[1,0,1]
	v_pk_fma_f32 v[20:21], v[214:215], v[24:25], v[20:21] op_sel_hi:[1,0,1]
	v_pk_fma_f32 v[14:15], v[212:213], v[28:29], v[14:15] op_sel_hi:[1,0,1]
	v_pk_fma_f32 v[16:17], v[214:215], v[28:29], v[16:17] op_sel_hi:[1,0,1]
	v_pk_fma_f32 v[10:11], v[212:213], v[32:33], v[10:11] op_sel_hi:[1,0,1]
	v_pk_fma_f32 v[12:13], v[214:215], v[32:33], v[12:13] op_sel_hi:[1,0,1]
	v_pk_fma_f32 v[6:7], v[212:213], v[94:95], v[6:7] op_sel_hi:[1,0,1]
	v_pk_fma_f32 v[8:9], v[214:215], v[94:95], v[8:9] op_sel_hi:[1,0,1]
	v_pk_fma_f32 v[2:3], v[212:213], v[98:99], v[2:3] op_sel_hi:[1,0,1]
	v_pk_fma_f32 v[4:5], v[214:215], v[98:99], v[4:5] op_sel_hi:[1,0,1]
	s_waitcnt vmcnt(4)
	v_pk_fma_f32 v[18:19], v[216:217], v[24:25], v[18:19] op_sel:[0,1,0]
	v_pk_fma_f32 v[20:21], v[218:219], v[24:25], v[20:21] op_sel:[0,1,0]
	v_pk_fma_f32 v[14:15], v[216:217], v[28:29], v[14:15] op_sel:[0,1,0]
	v_pk_fma_f32 v[16:17], v[218:219], v[28:29], v[16:17] op_sel:[0,1,0]
	v_pk_fma_f32 v[10:11], v[216:217], v[32:33], v[10:11] op_sel:[0,1,0]
	v_pk_fma_f32 v[12:13], v[218:219], v[32:33], v[12:13] op_sel:[0,1,0]
	v_pk_fma_f32 v[6:7], v[216:217], v[94:95], v[6:7] op_sel:[0,1,0]
	v_pk_fma_f32 v[8:9], v[218:219], v[94:95], v[8:9] op_sel:[0,1,0]
	v_pk_fma_f32 v[2:3], v[216:217], v[98:99], v[2:3] op_sel:[0,1,0]
	v_pk_fma_f32 v[4:5], v[218:219], v[98:99], v[4:5] op_sel:[0,1,0]
	s_waitcnt lgkmcnt(0)
	s_waitcnt vmcnt(3)
	v_pk_fma_f32 v[18:19], v[220:221], v[236:237], v[18:19] op_sel_hi:[1,0,1]
	v_pk_fma_f32 v[20:21], v[222:223], v[236:237], v[20:21] op_sel_hi:[1,0,1]
	v_pk_fma_f32 v[14:15], v[220:221], v[240:241], v[14:15] op_sel_hi:[1,0,1]
	v_pk_fma_f32 v[16:17], v[222:223], v[240:241], v[16:17] op_sel_hi:[1,0,1]
	v_pk_fma_f32 v[10:11], v[220:221], v[244:245], v[10:11] op_sel_hi:[1,0,1]
	v_pk_fma_f32 v[12:13], v[222:223], v[244:245], v[12:13] op_sel_hi:[1,0,1]
	v_pk_fma_f32 v[6:7], v[220:221], v[248:249], v[6:7] op_sel_hi:[1,0,1]
	v_pk_fma_f32 v[8:9], v[222:223], v[248:249], v[8:9] op_sel_hi:[1,0,1]
	v_pk_fma_f32 v[2:3], v[220:221], v[100:101], v[2:3] op_sel_hi:[1,0,1]
	v_pk_fma_f32 v[4:5], v[222:223], v[100:101], v[4:5] op_sel_hi:[1,0,1]
	s_waitcnt vmcnt(2)
	v_pk_fma_f32 v[18:19], v[224:225], v[236:237], v[18:19] op_sel:[0,1,0]
	v_pk_fma_f32 v[20:21], v[226:227], v[236:237], v[20:21] op_sel:[0,1,0]
	v_pk_fma_f32 v[14:15], v[224:225], v[240:241], v[14:15] op_sel:[0,1,0]
	v_pk_fma_f32 v[16:17], v[226:227], v[240:241], v[16:17] op_sel:[0,1,0]
	v_pk_fma_f32 v[10:11], v[224:225], v[244:245], v[10:11] op_sel:[0,1,0]
	v_pk_fma_f32 v[12:13], v[226:227], v[244:245], v[12:13] op_sel:[0,1,0]
	v_pk_fma_f32 v[6:7], v[224:225], v[248:249], v[6:7] op_sel:[0,1,0]
	v_pk_fma_f32 v[8:9], v[226:227], v[248:249], v[8:9] op_sel:[0,1,0]
	v_pk_fma_f32 v[2:3], v[224:225], v[100:101], v[2:3] op_sel:[0,1,0]
	v_pk_fma_f32 v[4:5], v[226:227], v[100:101], v[4:5] op_sel:[0,1,0]
	s_waitcnt vmcnt(1)
	v_pk_fma_f32 v[18:19], v[228:229], v[238:239], v[18:19] op_sel_hi:[1,0,1]
	v_pk_fma_f32 v[20:21], v[230:231], v[238:239], v[20:21] op_sel_hi:[1,0,1]
	v_pk_fma_f32 v[14:15], v[228:229], v[242:243], v[14:15] op_sel_hi:[1,0,1]
	v_pk_fma_f32 v[16:17], v[230:231], v[242:243], v[16:17] op_sel_hi:[1,0,1]
	v_pk_fma_f32 v[10:11], v[228:229], v[246:247], v[10:11] op_sel_hi:[1,0,1]
	v_pk_fma_f32 v[12:13], v[230:231], v[246:247], v[12:13] op_sel_hi:[1,0,1]
	v_pk_fma_f32 v[6:7], v[228:229], v[250:251], v[6:7] op_sel_hi:[1,0,1]
	v_pk_fma_f32 v[8:9], v[230:231], v[250:251], v[8:9] op_sel_hi:[1,0,1]
	v_pk_fma_f32 v[2:3], v[228:229], v[102:103], v[2:3] op_sel_hi:[1,0,1]
	v_pk_fma_f32 v[4:5], v[230:231], v[102:103], v[4:5] op_sel_hi:[1,0,1]
	s_waitcnt vmcnt(0)
	v_pk_fma_f32 v[18:19], v[232:233], v[238:239], v[18:19] op_sel:[0,1,0]
	v_pk_fma_f32 v[20:21], v[234:235], v[238:239], v[20:21] op_sel:[0,1,0]
	v_pk_fma_f32 v[14:15], v[232:233], v[242:243], v[14:15] op_sel:[0,1,0]
	v_pk_fma_f32 v[16:17], v[234:235], v[242:243], v[16:17] op_sel:[0,1,0]
	v_pk_fma_f32 v[10:11], v[232:233], v[246:247], v[10:11] op_sel:[0,1,0]
	v_pk_fma_f32 v[12:13], v[234:235], v[246:247], v[12:13] op_sel:[0,1,0]
	v_pk_fma_f32 v[6:7], v[232:233], v[250:251], v[6:7] op_sel:[0,1,0]
	v_pk_fma_f32 v[8:9], v[234:235], v[250:251], v[8:9] op_sel:[0,1,0]
	v_pk_fma_f32 v[2:3], v[232:233], v[102:103], v[2:3] op_sel:[0,1,0]
	v_pk_fma_f32 v[4:5], v[234:235], v[102:103], v[4:5] op_sel:[0,1,0]
	s_and_b32 s25, s26, 15
	s_lshl_b32 s25, s25, 1
	s_add_i32 s24, s25, s24
	s_mul_hi_i32 s25, s24, 0x3c000
	s_mul_i32 s24, s24, 0x3c000
	s_add_u32 s24, s37, s24
	s_addc_u32 s25, s38, s25
	s_add_u32 s22, s24, s22
	s_addc_u32 s23, s25, s23
	v_mov_b32_e32 v49, v37
	v_lshl_add_u64 v[22:23], s[22:23], 0, v[48:49]
	global_store_dwordx4 v48, v[18:21], s[22:23]
	s_nop 1
	v_add_co_u32_e32 v18, vcc, 0xc000, v22
	s_nop 1
	v_addc_co_u32_e32 v19, vcc, 0, v23, vcc
	global_store_dwordx4 v[18:19], v[14:17], off
	s_nop 1
	v_add_co_u32_e32 v14, vcc, 0x18000, v22
	s_nop 1
	v_addc_co_u32_e32 v15, vcc, 0, v23, vcc
	global_store_dwordx4 v[14:15], v[10:13], off
	s_nop 1
	v_add_co_u32_e32 v10, vcc, 0x24000, v22
	s_nop 1
	v_addc_co_u32_e32 v11, vcc, 0, v23, vcc
	global_store_dwordx4 v[10:11], v[6:9], off
	s_nop 1
	v_add_co_u32_e32 v6, vcc, 0x30000, v22
	s_nop 1
	v_addc_co_u32_e32 v7, vcc, 0, v23, vcc
	global_store_dwordx4 v[6:7], v[2:5], off
	s_branch .LBB0_28
